# RWKV scan: writer waves poll the progress word with s_sleep 6 instead of 1 so they take fewer issue / LDS slots from the scanning wave on their SIMD
# baseline (speedup 1.0000x reference)
.LBB0_1349:
	s_sleep 6
	ds_read_b32 v6, v5
	s_waitcnt lgkmcnt(0)
	v_cmp_ge_u32_e32 vcc, s11, v6
	s_cbranch_vccnz .LBB0_1349

.LBB0_1353:
	s_sleep 6
	ds_read_b32 v6, v5
	s_waitcnt lgkmcnt(0)
	v_cmp_ge_u32_e32 vcc, s13, v6
	s_cbranch_vccnz .LBB0_1353

.LBB0_3667:
	s_sleep 6
	ds_read_b32 v6, v5
	s_waitcnt lgkmcnt(0)
	v_cmp_ge_u32_e32 vcc, s14, v6
	s_cbranch_vccnz .LBB0_3667

.LBB0_3671:
	s_sleep 6
	ds_read_b32 v6, v5
	s_waitcnt lgkmcnt(0)
	v_cmp_ge_u32_e32 vcc, s10, v6
	s_cbranch_vccnz .LBB0_3671
